# P9+P10 MoE GEMM LDS tiles staged as full 128B lines per DMA (8 rows x 128B), XOR-swizzled fragment reads
# baseline (speedup 1.0000x reference)
; #define LAS __attribute__((address_space(3)))
;     __device__ __forceinline__ void prefetch(const Unit& u) const { if (u.e == 0) rs.prefetch(u); else cs.prefetch(u); }
;         u.e = v & 255; u.tl = (v >> 8) & 255; u.pn = (v >> 16) & 31; u.pm = (int)((unsigned)v >> 21);
;         u.a = GATHER ? A : A + (size_t)u.pm * 256 * 2048; u.b = Bt + ((size_t)u.e * brows + u.pn * 256) * 2048; return true; }
;     __device__ __forceinline__ void gather(const Unit& u, const unsigned (&voffA)[2], unsigned (&g)[2][2]) const {
;         const int ce = cnt[u.e];
; #pragma unroll
;         for (int i = 0; i < 2; ++i) { int R, C; stage_rc((int)threadIdx.x * 16 + i * 8192, R, C);
; #pragma unroll
;             for (int h = 0; h < 2; ++h) { const int pos = u.tl * 256 + h * 128 + R; const int pc = pos < ce ? pos : ce - 1; const int tok = list[2 * ((size_t)u.e * NTOK + pc)]; g[h][i] = (unsigned)tok * 2048u + voffA[i]; } }
;     __device__ __forceinline__ void prefetch(const Unit& u) const { const int tid = threadIdx.x, w = __builtin_amdgcn_readfirstlane(tid >> 6); LAS float* s = slots + (u.idx & 1) * 512 + w * 64; const float* g;
;         if (w < 4) { const int ce = cnt[u.e], pos = u.tl * 256 + tid, pc = pos < ce ? pos : ce - 1; g = (const float*)(list + 2 * ((size_t)u.e * NTOK + pc) + 1); }
;         else { const int c = tid - 256; g = b_gu + (size_t)u.e * 4096 + (c >> 7) * 2048 + u.pn * 128 + (c & 127); }
;         __builtin_amdgcn_global_load_lds((const unsigned*)g, (LAS unsigned*)s, 4, 0, 0); }
.LBB5_1585:
	s_add_i32 s0, 0, 0x20500
	v_mov_b32_e32 v1, s0
	ds_read_b32 v1, v1
	v_readfirstlane_b32 s14, v0
	s_waitcnt lgkmcnt(0)
	v_cmp_gt_i32_e32 vcc, 0, v1
	v_readfirstlane_b32 s8, v1
	s_cbranch_vccnz .LBB5_1614
	s_add_u32 s15, s22, 0xbc000000
	s_addc_u32 s27, s23, 0
	s_and_b32 s6, s8, 0xff
	s_lshl_b32 s0, s6, 2
	s_add_i32 s0, s0, 0
	s_add_i32 s0, s0, 0x20300
	s_waitcnt vmcnt(0)
	v_mov_b32_e32 v2, s0
	ds_read_b32 v2, v2
	v_lshrrev_b32_e32 v5, 3, v0
	v_bfe_u32 v1, v0, 3, 25
	v_bfe_u32 v4, v0, 2, 4
	v_or_b32_e32 v6, 64, v1
	s_and_b32 s9, s8, 0xff00
	v_mov_b32_e32 v1, v5
	s_waitcnt lgkmcnt(0)
	v_add_u32_e32 v7, -1, v2
	v_or_b32_e32 v8, s9, v1
	s_bfe_u32 s63, s8, 0x50010
	v_min_i32_e32 v2, v8, v7
	s_lshl_b32 s0, s6, 18
	v_or_b32_e32 v8, 0x80, v8
	s_movk_i32 s2, 0x70
	s_add_u32 s0, s15, s0
	v_min_i32_e32 v8, v8, v7
	v_mov_b32_e32 v199, v6
	s_addc_u32 s1, s27, 0
	v_ashrrev_i32_e32 v9, 31, v8
	v_or_b32_e32 v4, s9, v199
	v_lshl_add_u64 v[12:13], v[8:9], 3, s[0:1]
	v_min_i32_e32 v8, v4, v7
	v_or_b32_e32 v202, 0x80, v199
	v_ashrrev_i32_e32 v9, 31, v8
	v_or_b32_e32 v4, s9, v202
	v_ashrrev_i32_e32 v3, 31, v2
	v_lshl_add_u64 v[14:15], v[8:9], 3, s[0:1]
	v_min_i32_e32 v8, v4, v7
	v_lshl_add_u64 v[2:3], v[2:3], 3, s[0:1]
	v_ashrrev_i32_e32 v9, 31, v8
	v_lshl_add_u64 v[16:17], v[8:9], 3, s[0:1]
	global_load_dword v11, v[2:3], off
	global_load_dword v9, v[12:13], off
	global_load_dword v10, v[14:15], off
	global_load_dword v8, v[16:17], off
	v_readfirstlane_b32 s7, v0
	s_cmpk_gt_u32 s7, 0xff
	v_lshlrev_b32_e32 v4, 4, v0
	s_cbranch_scc0 .LBB5_1588
	v_readlane_b32 s36, v253, 2
	v_readlane_b32 s37, v253, 3
	s_lshl_b32 s2, s6, 14
	s_mov_b64 s[12:13], s[36:37]
	s_add_u32 s10, s12, s2
	v_and_b32_e32 v2, 0x1800, v4
	s_addc_u32 s11, s13, 0
	v_lshlrev_b32_e32 v2, 2, v2
	v_mov_b32_e32 v3, 0
	s_mov_b32 s3, 0
	v_lshl_add_u64 v[12:13], s[10:11], 0, v[2:3]
	s_lshl_b32 s2, s63, 9
	v_and_b32_e32 v2, 0x7f, v0
	v_lshl_add_u64 v[12:13], v[12:13], 0, s[2:3]
	v_lshlrev_b32_e32 v2, 2, v2
	s_movk_i32 s2, 0xc000
	v_lshl_add_u64 v[2:3], v[12:13], 0, v[2:3]
	s_mov_b32 s3, -1
	v_readlane_b32 s38, v253, 4
	v_readlane_b32 s39, v253, 5
	v_readlane_b32 s40, v253, 6
	v_readlane_b32 s41, v253, 7
	v_readlane_b32 s42, v253, 8
	v_readlane_b32 s43, v253, 9
	v_lshl_add_u64 v[2:3], v[2:3], 0, s[2:3]
	s_cbranch_execz .LBB5_1589
	s_branch .LBB5_1590

; #define PG8_STAGE(bufoff, gbase, voff) do { _Pragma("unroll") for (int _i = 0; _i < 2; ++_i) { unsigned _vo = (voff)[_i]; asm volatile("" : "+v"(_vo)); \
;         __builtin_amdgcn_global_load_lds((const unsigned*)((const char*)(gbase) + _vo), (LAS unsigned*)(lds + (bufoff) + ldsw + _i * 8192), 16, 0, 0); } } while (0)
; #define PG8_STAGE_A(bufoff, gbase, h, go) do { if constexpr (Sched::GATHER) { PG8_STAGE(bufoff, gbase, go[h]); } else { PG8_STAGE(bufoff, (gbase) + (h) * hstep, voffA); } } while (0)
; #define PG8_WAIT_V(n) asm volatile("s_waitcnt vmcnt(" #n ")" ::: "memory")
; #define PG8_BAR __builtin_amdgcn_s_barrier()
;     ...
;     const int tid = threadIdx.x, wid = __builtin_amdgcn_readfirstlane(tid >> 6), lane = tid & 63, wr = wid >> 2, wc = wid & 3, fr = lane & 15, fq = lane >> 4;
;     const int nt = KB / 128;
;     unsigned voffA[2], voffB[2];
; #pragma unroll
;     for (int i = 0; i < 2; ++i) { int R, C; stage_rc(tid * 16 + i * 8192, R, C); const int Rb = Epi::PERM ? ((R & ~31) + perm32(R & 31)) : R;
;         voffA[i] = Sched::GATHER ? (unsigned)(C * 2) : (unsigned)(R * KB + C * 2); voffB[i] = (unsigned)(Rb * KB + C * 2); }
;     const size_t kstep = (size_t)(BK * 2);
;     const size_t hstep = (size_t)HALF * KB;
;     const unsigned ldsw = (unsigned)wid * 1024u;
;     const int aoff = lds_byte(wr * 64 + fr, fq * 8), boff = lds_byte(wc * 32 + fr, fq * 8);
;     ...
;     Unit cur, nxt; int ui = 0;
;     if (!S.next(0, cur)) return;
;     Acc acc;
; #pragma unroll
;     for (int a = 0; a < 2; ++a)
; #pragma unroll
;         for (int b = 0; b < 2; ++b)
; #pragma unroll
;             for (int m = 0; m < 4; ++m)
; #pragma unroll
;                 for (int n = 0; n < 2; ++n) acc[a][b][m][n] = (f32x4){0.f, 0.f, 0.f, 0.f};
;     bf16x8 At[4][2], B0[2][2], B1[2][2];
;     const char* cA = cur.a; const char* cB = cur.b;
;     unsigned gc[2][2], gn[2][2];
;     if constexpr (Sched::GATHER) { S.gather(cur, voffA, gc); }
;     if constexpr (Epi::PREF) E.prefetch(cur);
;     PG8_STAGE(PG8_SB(0, 0), cB, voffB); PG8_STAGE(PG8_SB(0, 1), cB + hstep, voffB); PG8_STAGE_A(PG8_SA(0, 0), cA, 0, gc); PG8_STAGE_A(PG8_SA(0, 1), cA, 1, gc);
;     if (wr == 1) PG8_BAR;
;     PG8_WAIT_V(2); PG8_BAR;
;     PG8_STAGE(PG8_SB(1, 0), cB + kstep, voffB); PG8_STAGE_A(PG8_SA(1, 0), cA + kstep, 0, gc); PG8_STAGE(PG8_SB(1, 1), cB + hstep + kstep, voffB);
;     PG8_WAIT_V(6); PG8_BAR;
.LBB5_1590:
	s_add_u32 s29, s22, 0x8000000
	s_addc_u32 s42, s23, 0
	v_lshrrev_b32_e32 v7, 4, v0
	s_lshl_b32 s0, s63, 19
	s_lshl_b32 s1, s6, 23
	v_xor_b32_e32 v7, v7, v0
	s_add_u32 s1, s29, s1
	v_and_b32_e32 v7, 7, v7
	s_addc_u32 s2, s42, 0
	v_lshlrev_b32_e32 v203, 4, v7
	s_add_u32 s38, s1, s0
	s_waitcnt vmcnt(0)
	v_lshl_or_b32 v206, v8, 11, v203
	v_and_b32_e32 v7, 0x23, v5
	v_and_b32_e32 v8, 12, v5
	s_addc_u32 s39, s2, 0
	v_lshl_or_b32 v204, v9, 11, v203
	v_lshl_or_b32 v7, v8, 1, v7
	v_bfe_u32 v8, v5, 4, 1
	s_add_u32 s2, s22, 0x60000000
	v_lshl_or_b32 v7, v8, 2, v7
	s_addc_u32 s3, s23, 0
	s_movk_i32 s1, 0x60
	s_and_b32 s6, s7, 0x3fffffc0
	v_lshl_or_b32 v208, v7, 11, v203
	v_or_b32_e32 v5, 64, v7
	s_lshr_b32 s1, s14, 6
	s_lshl_b32 s6, s6, 2
	s_lshl_b32 s43, s1, 10
	s_add_i32 s6, s6, 0
	s_add_i32 m0, s6, 0x20800
	s_add_i32 s44, s43, 0
	global_load_lds_dword v[2:3], off
	s_add_i32 s45, s44, 0x10000
	v_mov_b32_e32 v2, v208
	v_lshl_or_b32 v209, v5, 11, v203
	s_mov_b32 m0, s45
	s_lshr_b32 s0, s14, 8
	global_load_lds_dwordx4 v2, s[38:39]
	v_mov_b32_e32 v2, v209
	s_add_i32 s46, s44, 0x12000
	s_mov_b32 m0, s46
	s_add_u32 s6, s38, 0x40000
	global_load_lds_dwordx4 v2, s[38:39]
	s_addc_u32 s7, s39, 0
	s_add_i32 s47, s44, 0x14000
	v_mov_b32_e32 v2, v208
	s_mov_b32 m0, s47
	s_add_i32 s48, s44, 0x16000
	global_load_lds_dwordx4 v2, s[6:7]
	v_mov_b32_e32 v2, v209
	v_lshl_or_b32 v205, v11, 11, v203
	s_mov_b32 m0, s48
	v_lshl_or_b32 v207, v10, 11, v203
	global_load_lds_dwordx4 v2, s[6:7]
	v_mov_b32_e32 v2, v205
	s_mov_b32 m0, s44
	s_add_i32 s49, s44, 0x2000
	global_load_lds_dwordx4 v2, s[2:3]
	v_mov_b32_e32 v2, v207
	s_mov_b32 m0, s49
	s_add_i32 s50, s44, 0x4000
	global_load_lds_dwordx4 v2, s[2:3]
	v_mov_b32_e32 v2, v204
	s_mov_b32 m0, s50
	s_add_i32 s51, s44, 0x6000
	global_load_lds_dwordx4 v2, s[2:3]
	v_mov_b32_e32 v2, v206
	s_mov_b32 m0, s51
	s_cmp_eq_u32 s0, 1
	global_load_lds_dwordx4 v2, s[2:3]
	s_cselect_b64 s[6:7], -1, 0
	s_cmp_lg_u32 s0, 1
	s_mov_b32 s65, 0
	s_cbranch_scc1 .LBB5_1592
	s_barrier
.LBB5_1592:
	s_lshr_b32 s64, s8, 21
	s_add_u32 s8, s22, 0x68000000
	v_mov_b32_e32 v194, v208
	v_mov_b32_e32 v195, 0
	s_addc_u32 s9, s23, 0
	s_lshl_b32 s52, s0, 6
	s_lshl_b32 s12, s0, 13
	s_lshl_b32 s0, s1, 5
	s_waitcnt vmcnt(2)
	s_barrier
	s_mov_b64 s[10:11], 0x80
	v_lshl_add_u64 v[2:3], s[38:39], 0, v[194:195]
	s_and_b32 s53, s0, 0x60
	s_add_i32 m0, s44, 0x18000
	v_lshl_add_u64 v[2:3], v[2:3], 0, s[10:11]
	v_mov_b32_e32 v194, v209
	s_lshl_b32 s13, s53, 7
	global_load_lds_dwordx4 v[2:3], off
	s_add_i32 m0, s44, 0x1a000
	v_lshl_add_u64 v[2:3], s[38:39], 0, v[194:195]
	v_lshl_add_u64 v[2:3], v[2:3], 0, s[10:11]
	s_add_u32 s0, s22, 0x60000080
	global_load_lds_dwordx4 v[2:3], off
	s_addc_u32 s1, s23, 0
	v_mov_b32_e32 v2, v205
	s_add_i32 s54, s44, 0x8000
	s_mov_b32 m0, s54
	s_add_i32 s55, s44, 0xa000
	global_load_lds_dwordx4 v2, s[0:1]
	v_mov_b32_e32 v2, v207
	s_mov_b32 m0, s55
	v_bfe_u32 v211, v0, 4, 2
	global_load_lds_dwordx4 v2, s[0:1]
	s_add_u32 s0, s38, 0x40080
	v_mov_b32_e32 v2, v208
	s_addc_u32 s1, s39, 0
	s_add_i32 m0, s44, 0x1c000
	v_and_b32_e32 v210, 15, v0
	global_load_lds_dwordx4 v2, s[0:1]
	v_mov_b32_e32 v2, v209
	s_add_i32 m0, s44, 0x1e000
	v_lshrrev_b32_e32 v5, 1, v210
	global_load_lds_dwordx4 v2, s[0:1]
	v_xor_b32_e32 v2, v5, v211
	v_lshlrev_b32_e32 v2, 4, v2
	s_movk_i32 s0, 0x3c0
	v_lshl_or_b32 v3, v210, 7, v2
	v_or_b32_e32 v212, s13, v3
	s_waitcnt vmcnt(6)
	v_and_b32_e32 v4, 0x1800, v4
	v_readlane_b32 s68, v253, 2
	v_or_b32_e32 v3, s12, v3
	s_cmpk_lt_u32 s14, 0x100
	v_and_b32_e32 v2, 0x7f, v0
	v_lshlrev_b32_e32 v194, 2, v4
	v_readlane_b32 s69, v253, 3
	v_add_u32_e32 v4, 0, v212
	s_movk_i32 s16, 0xc000
	s_cselect_b64 s[12:13], -1, 0
	s_and_b32 s56, s14, 0xffffff00
	v_lshl_add_u64 v[196:197], s[68:69], 0, v[194:195]
	v_add_u32_e32 v213, 0x10000, v4
	v_add_u32_e32 v214, 0x14000, v4
	v_add_u32_e32 v215, 0, v3
	v_mov_b32_e32 v216, 0x7c7c7c7c
	s_mov_b32 s57, 0xc0e00000
	s_mov_b32 s14, 0xc01d265f
	v_lshlrev_b32_e32 v200, 2, v2
	s_mov_b32 s17, -1
	v_mov_b32_e32 v217, 0x40e00000
	s_mov_b32 s61, 0
	s_barrier
	v_readlane_b32 s70, v253, 4
	v_readlane_b32 s71, v253, 5
	v_readlane_b32 s72, v253, 6
	v_readlane_b32 s73, v253, 7
	v_readlane_b32 s74, v253, 8
	v_readlane_b32 s75, v253, 9
	s_branch .LBB5_1595

; #define PG8_STAGE(bufoff, gbase, voff) do { _Pragma("unroll") for (int _i = 0; _i < 2; ++_i) { unsigned _vo = (voff)[_i]; asm volatile("" : "+v"(_vo)); \
;         __builtin_amdgcn_global_load_lds((const unsigned*)((const char*)(gbase) + _vo), (LAS unsigned*)(lds + (bufoff) + ldsw + _i * 8192), 16, 0, 0); } } while (0)
; #define PG8_STAGE_A(bufoff, gbase, h, go) do { if constexpr (Sched::GATHER) { PG8_STAGE(bufoff, gbase, go[h]); } else { PG8_STAGE(bufoff, (gbase) + (h) * hstep, voffA); } } while (0)
; #define PG8_LDA(dst, b, h) do { _Pragma("unroll") for (int m = 0; m < 4; ++m) _Pragma("unroll") for (int k = 0; k < 2; ++k) dst[m][k] = *(const LAS bf16x8*)(lds + PG8_SA(b, h) + aoff + m * 2048 + k * 1024); } while (0)
; #define PG8_LDB(dst, b, h) do { _Pragma("unroll") for (int n = 0; n < 2; ++n) _Pragma("unroll") for (int k = 0; k < 2; ++k) dst[n][k] = *(const LAS bf16x8*)(lds + PG8_SB(b, h) + boff + n * 2048 + k * 1024); } while (0)
; #define PG8_WAIT_V(n) asm volatile("s_waitcnt vmcnt(" #n ")" ::: "memory")
; #define PG8_WAIT_L(n) asm volatile("s_waitcnt lgkmcnt(" #n ")" ::: "memory")
; #define PG8_BAR __builtin_amdgcn_s_barrier()
;     ...
;             PG8_LDB(B0, 0, 0); PG8_LDB(B1, 0, 1); PG8_SCHED; PG8_LDA(At, 0, 0); PG8_STAGE_A(PG8_SA(1, 1), a1, 1, gc);
;             if constexpr (Sched::GATHER) { if (last) {
; #pragma unroll
;                 for (int h = 0; h < 2; ++h)
; #pragma unroll
;                     for (int i = 0; i < 2; ++i) gc[h][i] = gn[h][i]; } }
;             PG8_WAIT_V(8); PG8_WAIT_L(0); PG8_BAR; PG8_MMA(0, 0, At, B0); PG8_MMA(0, 1, At, B1); PG8_BAR; PG8_SCHED;
;             PG8_LDA(At, 0, 1); PG8_STAGE(PG8_SB(0, 0), b2, voffB); PG8_STAGE(PG8_SB(0, 1), b2 + hstep, voffB); PG8_STAGE_A(PG8_SA(0, 0), a2, 0, gc);
;             PG8_WAIT_V(8); PG8_WAIT_L(0); PG8_BAR; PG8_MMA(1, 0, At, B0); PG8_MMA(1, 1, At, B1); PG8_BAR; PG8_SCHED;
;             PG8_LDB(B0, 1, 0); PG8_LDB(B1, 1, 1); PG8_SCHED; PG8_LDA(At, 1, 0); PG8_STAGE_A(PG8_SA(0, 1), a2, 1, gc);
;             PG8_WAIT_V(8); PG8_WAIT_L(0); PG8_BAR; PG8_MMA(0, 0, At, B0); PG8_MMA(0, 1, At, B1); PG8_BAR; PG8_SCHED;
;             PG8_LDA(At, 1, 1); PG8_STAGE(PG8_SB(1, 0), b3, voffB); PG8_STAGE(PG8_SB(1, 1), b3 + hstep, voffB); PG8_STAGE_A(PG8_SA(1, 0), a3, 0, gc);
;             PG8_WAIT_V(8); PG8_WAIT_L(0); PG8_BAR; PG8_MMA(1, 0, At, B0); PG8_MMA(1, 1, At, B1); PG8_BAR; PG8_SCHED;
;         }
.LBB5_1601:
	s_waitcnt vmcnt(8)
	s_add_u32 s40, s36, 0x80
	s_waitcnt lgkmcnt(0)
	s_addc_u32 s41, s37, 0
	s_and_b64 s[38:39], s[38:39], exec
	s_cselect_b32 s39, s19, s41
	s_cselect_b32 s38, s66, s40
	s_cselect_b32 s41, s67, s70
	s_cselect_b32 s40, s68, s69
	s_barrier
	s_setprio 1
	s_waitcnt lgkmcnt(0)
	v_mfma_scale_f32_16x16x128_f8f6f4 v[190:193], v[18:25], v[58:65], v[190:193], v216, v216 op_sel_hi:[0,0,0]
	v_mfma_scale_f32_16x16x128_f8f6f4 v[186:189], v[26:33], v[58:65], v[186:189], v216, v216 op_sel_hi:[0,0,0]
	v_mfma_scale_f32_16x16x128_f8f6f4 v[174:177], v[18:25], v[50:57], v[174:177], v216, v216 op_sel_hi:[0,0,0]
	v_mfma_scale_f32_16x16x128_f8f6f4 v[170:173], v[26:33], v[50:57], v[170:173], v216, v216 op_sel_hi:[0,0,0]
	v_mfma_scale_f32_16x16x128_f8f6f4 v[158:161], v[18:25], v[42:49], v[158:161], v216, v216 op_sel_hi:[0,0,0]
	v_mfma_scale_f32_16x16x128_f8f6f4 v[154:157], v[26:33], v[42:49], v[154:157], v216, v216 op_sel_hi:[0,0,0]
	v_mfma_scale_f32_16x16x128_f8f6f4 v[142:145], v[18:25], v[34:41], v[142:145], v216, v216 op_sel_hi:[0,0,0]
	v_mfma_scale_f32_16x16x128_f8f6f4 v[138:141], v[26:33], v[34:41], v[138:141], v216, v216 op_sel_hi:[0,0,0]
	s_setprio 0
	s_setprio 1
	v_mfma_scale_f32_16x16x128_f8f6f4 v[182:185], v[2:9], v[58:65], v[182:185], v216, v216 op_sel_hi:[0,0,0]
	v_mfma_scale_f32_16x16x128_f8f6f4 v[178:181], v[10:17], v[58:65], v[178:181], v216, v216 op_sel_hi:[0,0,0]
	v_mfma_scale_f32_16x16x128_f8f6f4 v[166:169], v[2:9], v[50:57], v[166:169], v216, v216 op_sel_hi:[0,0,0]
	v_mfma_scale_f32_16x16x128_f8f6f4 v[162:165], v[10:17], v[50:57], v[162:165], v216, v216 op_sel_hi:[0,0,0]
	v_mfma_scale_f32_16x16x128_f8f6f4 v[150:153], v[2:9], v[42:49], v[150:153], v216, v216 op_sel_hi:[0,0,0]
	v_mfma_scale_f32_16x16x128_f8f6f4 v[146:149], v[10:17], v[42:49], v[146:149], v216, v216 op_sel_hi:[0,0,0]
	v_mfma_scale_f32_16x16x128_f8f6f4 v[134:137], v[2:9], v[34:41], v[134:137], v216, v216 op_sel_hi:[0,0,0]
	v_mfma_scale_f32_16x16x128_f8f6f4 v[130:133], v[10:17], v[34:41], v[130:133], v216, v216 op_sel_hi:[0,0,0]
	s_setprio 0
	s_barrier
	v_mov_b32_e32 v194, v208
	s_mov_b32 m0, s45
	ds_read_b128 v[38:41], v215 offset:16384
	ds_read_b128 v[46:49], v215 offset:18432
	ds_read_b128 v[54:57], v215 offset:20480
	ds_read_b128 v[62:65], v215 offset:22528
	v_xor_b32_e32 v215, 64, v215
	ds_read_b128 v[34:37], v215 offset:16384
	ds_read_b128 v[42:45], v215 offset:18432
	ds_read_b128 v[50:53], v215 offset:20480
	ds_read_b128 v[58:61], v215 offset:22528
	s_add_u32 s72, s40, 0x40000
	global_load_lds_dwordx4 v194, s[40:41]
	v_mov_b32_e32 v194, v209
	s_mov_b32 m0, s46
	s_addc_u32 s73, s41, 0
	global_load_lds_dwordx4 v194, s[40:41]
	v_mov_b32_e32 v194, v208
	s_mov_b32 m0, s47
	s_nop 0
	global_load_lds_dwordx4 v194, s[72:73]
	v_mov_b32_e32 v194, v209
	s_mov_b32 m0, s48
	s_nop 0
	global_load_lds_dwordx4 v194, s[72:73]
	v_mov_b32_e32 v194, v205
	s_mov_b32 m0, s44
	s_nop 0
	global_load_lds_dwordx4 v194, s[38:39]
	v_mov_b32_e32 v194, v207
	s_mov_b32 m0, s49
	s_nop 0
	global_load_lds_dwordx4 v194, s[38:39]
	s_waitcnt vmcnt(8)
	s_waitcnt lgkmcnt(0)
	s_barrier
	s_setprio 1
	s_waitcnt lgkmcnt(0)
	v_mfma_scale_f32_16x16x128_f8f6f4 v[126:129], v[18:25], v[34:41], v[126:129], v216, v216 op_sel_hi:[0,0,0]
	v_mfma_scale_f32_16x16x128_f8f6f4 v[122:125], v[26:33], v[34:41], v[122:125], v216, v216 op_sel_hi:[0,0,0]
	v_mfma_scale_f32_16x16x128_f8f6f4 v[110:113], v[18:25], v[42:49], v[110:113], v216, v216 op_sel_hi:[0,0,0]
	v_mfma_scale_f32_16x16x128_f8f6f4 v[106:109], v[26:33], v[42:49], v[106:109], v216, v216 op_sel_hi:[0,0,0]
	v_mfma_scale_f32_16x16x128_f8f6f4 v[94:97], v[18:25], v[50:57], v[94:97], v216, v216 op_sel_hi:[0,0,0]
	v_mfma_scale_f32_16x16x128_f8f6f4 v[90:93], v[26:33], v[50:57], v[90:93], v216, v216 op_sel_hi:[0,0,0]
	v_mfma_scale_f32_16x16x128_f8f6f4 v[78:81], v[18:25], v[58:65], v[78:81], v216, v216 op_sel_hi:[0,0,0]
	v_mfma_scale_f32_16x16x128_f8f6f4 v[74:77], v[26:33], v[58:65], v[74:77], v216, v216 op_sel_hi:[0,0,0]
	s_setprio 0
	s_setprio 1
	v_mfma_scale_f32_16x16x128_f8f6f4 v[118:121], v[2:9], v[34:41], v[118:121], v216, v216 op_sel_hi:[0,0,0]
	v_mfma_scale_f32_16x16x128_f8f6f4 v[114:117], v[10:17], v[34:41], v[114:117], v216, v216 op_sel_hi:[0,0,0]
	v_mfma_scale_f32_16x16x128_f8f6f4 v[102:105], v[2:9], v[42:49], v[102:105], v216, v216 op_sel_hi:[0,0,0]
	v_mfma_scale_f32_16x16x128_f8f6f4 v[98:101], v[10:17], v[42:49], v[98:101], v216, v216 op_sel_hi:[0,0,0]
	v_mfma_scale_f32_16x16x128_f8f6f4 v[86:89], v[2:9], v[50:57], v[86:89], v216, v216 op_sel_hi:[0,0,0]
	v_mfma_scale_f32_16x16x128_f8f6f4 v[82:85], v[10:17], v[50:57], v[82:85], v216, v216 op_sel_hi:[0,0,0]
	v_mfma_scale_f32_16x16x128_f8f6f4 v[70:73], v[2:9], v[58:65], v[70:73], v216, v216 op_sel_hi:[0,0,0]
	v_mfma_scale_f32_16x16x128_f8f6f4 v[66:69], v[10:17], v[58:65], v[66:69], v216, v216 op_sel_hi:[0,0,0]
	s_setprio 0
	s_barrier
	s_add_i32 s72, 0, 0x18000
	s_add_i32 s73, 0, 0x1c000
	v_add_u32_e32 v14, s72, v212
	v_add_u32_e32 v30, s73, v212
	ds_read_b128 v[2:5], v14
	ds_read_b128 v[10:13], v14 offset:2048
	v_xor_b32_e32 v14, 64, v14
	ds_read_b128 v[6:9], v14
	ds_read_b128 v[14:17], v14 offset:2048
	ds_read_b128 v[18:21], v30
	ds_read_b128 v[26:29], v30 offset:2048
	v_xor_b32_e32 v30, 64, v30
	ds_read_b128 v[22:25], v30
	ds_read_b128 v[30:33], v30 offset:2048
	v_mov_b32_e32 v194, v204
	s_mov_b32 m0, s50
	ds_read_b128 v[34:37], v215 offset:32768
	ds_read_b128 v[42:45], v215 offset:34816
	ds_read_b128 v[50:53], v215 offset:36864
	ds_read_b128 v[58:61], v215 offset:38912
	v_xor_b32_e32 v215, 64, v215
	ds_read_b128 v[38:41], v215 offset:32768
	ds_read_b128 v[46:49], v215 offset:34816
	ds_read_b128 v[54:57], v215 offset:36864
	ds_read_b128 v[62:65], v215 offset:38912
	s_nop 0
	global_load_lds_dwordx4 v194, s[38:39]
	v_mov_b32_e32 v194, v206
	s_mov_b32 m0, s51
	s_nop 0
	global_load_lds_dwordx4 v194, s[38:39]
	s_waitcnt vmcnt(8)
	s_waitcnt lgkmcnt(0)
	s_barrier
; #define PG8_STAGE(bufoff, gbase, voff) do { _Pragma("unroll") for (int _i = 0; _i < 2; ++_i) { unsigned _vo = (voff)[_i]; asm volatile("" : "+v"(_vo)); \
;         __builtin_amdgcn_global_load_lds((const unsigned*)((const char*)(gbase) + _vo), (LAS unsigned*)(lds + (bufoff) + ldsw + _i * 8192), 16, 0, 0); } } while (0)
; #define PG8_STAGE_A(bufoff, gbase, h, go) do { if constexpr (Sched::GATHER) { PG8_STAGE(bufoff, gbase, go[h]); } else { PG8_STAGE(bufoff, (gbase) + (h) * hstep, voffA); } } while (0)
; #define PG8_LDA(dst, b, h) do { _Pragma("unroll") for (int m = 0; m < 4; ++m) _Pragma("unroll") for (int k = 0; k < 2; ++k) dst[m][k] = *(const LAS bf16x8*)(lds + PG8_SA(b, h) + aoff + m * 2048 + k * 1024); } while (0)
; #define PG8_LDB(dst, b, h) do { _Pragma("unroll") for (int n = 0; n < 2; ++n) _Pragma("unroll") for (int k = 0; k < 2; ++k) dst[n][k] = *(const LAS bf16x8*)(lds + PG8_SB(b, h) + boff + n * 2048 + k * 1024); } while (0)
; #define PG8_WAIT_V(n) asm volatile("s_waitcnt vmcnt(" #n ")" ::: "memory")
; #define PG8_WAIT_L(n) asm volatile("s_waitcnt lgkmcnt(" #n ")" ::: "memory")
; #define PG8_BAR __builtin_amdgcn_s_barrier()
; #define PG8_SCHED __builtin_amdgcn_sched_barrier(0)
;     ...
;             PG8_LDB(B0, 0, 0); PG8_LDB(B1, 0, 1); PG8_SCHED; PG8_LDA(At, 0, 0); PG8_STAGE_A(PG8_SA(1, 1), a1, 1, gc);
;             if constexpr (Sched::GATHER) { if (last) {
; #pragma unroll
;                 for (int h = 0; h < 2; ++h)
; #pragma unroll
;                     for (int i = 0; i < 2; ++i) gc[h][i] = gn[h][i]; } }
;     ...
;             PG8_WAIT_V(8); PG8_WAIT_L(0); PG8_BAR; PG8_MMA(1, 0, At, B0); PG8_MMA(1, 1, At, B1); PG8_BAR; PG8_SCHED;
;             PG8_LDB(B0, 1, 0); PG8_LDB(B1, 1, 1); PG8_SCHED; PG8_LDA(At, 1, 0); PG8_STAGE_A(PG8_SA(0, 1), a2, 1, gc);
;             PG8_WAIT_V(8); PG8_WAIT_L(0); PG8_BAR; PG8_MMA(0, 0, At, B0); PG8_MMA(0, 1, At, B1); PG8_BAR; PG8_SCHED;
;             PG8_LDA(At, 1, 1); PG8_STAGE(PG8_SB(1, 0), b3, voffB); PG8_STAGE(PG8_SB(1, 1), b3 + hstep, voffB); PG8_STAGE_A(PG8_SA(1, 0), a3, 0, gc);
;             PG8_WAIT_V(8); PG8_WAIT_L(0); PG8_BAR; PG8_MMA(1, 0, At, B0); PG8_MMA(1, 1, At, B1); PG8_BAR; PG8_SCHED;
;         }
	s_setprio 1
	s_waitcnt lgkmcnt(0)
	v_mfma_scale_f32_16x16x128_f8f6f4 v[190:193], v[2:9], v[34:41], v[190:193], v216, v216 op_sel_hi:[0,0,0]
	v_mfma_scale_f32_16x16x128_f8f6f4 v[186:189], v[10:17], v[34:41], v[186:189], v216, v216 op_sel_hi:[0,0,0]
	v_mfma_scale_f32_16x16x128_f8f6f4 v[174:177], v[2:9], v[42:49], v[174:177], v216, v216 op_sel_hi:[0,0,0]
	v_mfma_scale_f32_16x16x128_f8f6f4 v[170:173], v[10:17], v[42:49], v[170:173], v216, v216 op_sel_hi:[0,0,0]
	v_mfma_scale_f32_16x16x128_f8f6f4 v[158:161], v[2:9], v[50:57], v[158:161], v216, v216 op_sel_hi:[0,0,0]
	v_mfma_scale_f32_16x16x128_f8f6f4 v[154:157], v[10:17], v[50:57], v[154:157], v216, v216 op_sel_hi:[0,0,0]
	v_mfma_scale_f32_16x16x128_f8f6f4 v[142:145], v[2:9], v[58:65], v[142:145], v216, v216 op_sel_hi:[0,0,0]
	v_mfma_scale_f32_16x16x128_f8f6f4 v[138:141], v[10:17], v[58:65], v[138:141], v216, v216 op_sel_hi:[0,0,0]
	s_setprio 0
	s_setprio 1
	v_mfma_scale_f32_16x16x128_f8f6f4 v[182:185], v[18:25], v[34:41], v[182:185], v216, v216 op_sel_hi:[0,0,0]
	v_mfma_scale_f32_16x16x128_f8f6f4 v[178:181], v[26:33], v[34:41], v[178:181], v216, v216 op_sel_hi:[0,0,0]
	v_mfma_scale_f32_16x16x128_f8f6f4 v[166:169], v[18:25], v[42:49], v[166:169], v216, v216 op_sel_hi:[0,0,0]
	v_mfma_scale_f32_16x16x128_f8f6f4 v[162:165], v[26:33], v[42:49], v[162:165], v216, v216 op_sel_hi:[0,0,0]
	v_mfma_scale_f32_16x16x128_f8f6f4 v[150:153], v[18:25], v[50:57], v[150:153], v216, v216 op_sel_hi:[0,0,0]
	v_mfma_scale_f32_16x16x128_f8f6f4 v[146:149], v[26:33], v[50:57], v[146:149], v216, v216 op_sel_hi:[0,0,0]
	v_mfma_scale_f32_16x16x128_f8f6f4 v[134:137], v[18:25], v[58:65], v[134:137], v216, v216 op_sel_hi:[0,0,0]
	v_mfma_scale_f32_16x16x128_f8f6f4 v[130:133], v[26:33], v[58:65], v[130:133], v216, v216 op_sel_hi:[0,0,0]
	s_setprio 0
	s_barrier
	v_mov_b32_e32 v194, v208
	ds_read_b128 v[38:41], v215 offset:49152
	ds_read_b128 v[46:49], v215 offset:51200
	ds_read_b128 v[54:57], v215 offset:53248
	ds_read_b128 v[62:65], v215 offset:55296
	v_xor_b32_e32 v215, 64, v215
	ds_read_b128 v[34:37], v215 offset:49152
	ds_read_b128 v[42:45], v215 offset:51200
	ds_read_b128 v[50:53], v215 offset:53248
	ds_read_b128 v[58:61], v215 offset:55296
	s_add_i32 s72, s72, s43
	v_lshl_add_u64 v[222:223], s[40:41], 0, v[194:195]
	v_lshl_add_u64 v[222:223], v[222:223], 0, s[10:11]
	s_mov_b32 m0, s72
	v_mov_b32_e32 v194, v209
	global_load_lds_dwordx4 v[222:223], off
	s_add_i32 m0, s72, 0x2000
	s_nop 0
	v_lshl_add_u64 v[222:223], s[40:41], 0, v[194:195]
	s_add_u32 s40, s40, 0x40080
	v_lshl_add_u64 v[222:223], v[222:223], 0, s[10:11]
	s_addc_u32 s41, s41, 0
	v_mov_b32_e32 v194, v208
	s_add_i32 s72, s73, s43
	global_load_lds_dwordx4 v[222:223], off
	s_mov_b32 m0, s72
	s_nop 0
	global_load_lds_dwordx4 v194, s[40:41]
	v_mov_b32_e32 v194, v209
	s_add_i32 m0, s72, 0x2000
	s_nop 0
	global_load_lds_dwordx4 v194, s[40:41]
	v_mov_b32_e32 v194, v205
	s_mov_b32 m0, s54
	v_lshl_add_u64 v[222:223], s[38:39], 0, v[194:195]
	v_lshl_add_u64 v[222:223], v[222:223], 0, s[10:11]
	v_mov_b32_e32 v194, v207
	global_load_lds_dwordx4 v[222:223], off
	s_mov_b32 m0, s55
	v_lshl_add_u64 v[222:223], s[38:39], 0, v[194:195]
	v_lshl_add_u64 v[222:223], v[222:223], 0, s[10:11]
	global_load_lds_dwordx4 v[222:223], off
	s_waitcnt vmcnt(8)
	s_waitcnt lgkmcnt(0)
	s_barrier
	s_setprio 1
	s_waitcnt lgkmcnt(0)
	v_mfma_scale_f32_16x16x128_f8f6f4 v[126:129], v[2:9], v[34:41], v[126:129], v216, v216 op_sel_hi:[0,0,0]
	v_mfma_scale_f32_16x16x128_f8f6f4 v[122:125], v[10:17], v[34:41], v[122:125], v216, v216 op_sel_hi:[0,0,0]
	v_mfma_scale_f32_16x16x128_f8f6f4 v[110:113], v[2:9], v[42:49], v[110:113], v216, v216 op_sel_hi:[0,0,0]
	v_mfma_scale_f32_16x16x128_f8f6f4 v[106:109], v[10:17], v[42:49], v[106:109], v216, v216 op_sel_hi:[0,0,0]
	v_mfma_scale_f32_16x16x128_f8f6f4 v[94:97], v[2:9], v[50:57], v[94:97], v216, v216 op_sel_hi:[0,0,0]
	v_mfma_scale_f32_16x16x128_f8f6f4 v[90:93], v[10:17], v[50:57], v[90:93], v216, v216 op_sel_hi:[0,0,0]
	v_mfma_scale_f32_16x16x128_f8f6f4 v[78:81], v[2:9], v[58:65], v[78:81], v216, v216 op_sel_hi:[0,0,0]
	v_mfma_scale_f32_16x16x128_f8f6f4 v[74:77], v[10:17], v[58:65], v[74:77], v216, v216 op_sel_hi:[0,0,0]
	s_setprio 0
	s_setprio 1
	v_mfma_scale_f32_16x16x128_f8f6f4 v[118:121], v[18:25], v[34:41], v[118:121], v216, v216 op_sel_hi:[0,0,0]
	v_mfma_scale_f32_16x16x128_f8f6f4 v[114:117], v[26:33], v[34:41], v[114:117], v216, v216 op_sel_hi:[0,0,0]
	v_mfma_scale_f32_16x16x128_f8f6f4 v[102:105], v[18:25], v[42:49], v[102:105], v216, v216 op_sel_hi:[0,0,0]
	v_mfma_scale_f32_16x16x128_f8f6f4 v[98:101], v[26:33], v[42:49], v[98:101], v216, v216 op_sel_hi:[0,0,0]
	v_mfma_scale_f32_16x16x128_f8f6f4 v[86:89], v[18:25], v[50:57], v[86:89], v216, v216 op_sel_hi:[0,0,0]
	v_mfma_scale_f32_16x16x128_f8f6f4 v[82:85], v[26:33], v[50:57], v[82:85], v216, v216 op_sel_hi:[0,0,0]
	v_mfma_scale_f32_16x16x128_f8f6f4 v[70:73], v[18:25], v[58:65], v[70:73], v216, v216 op_sel_hi:[0,0,0]
	v_mfma_scale_f32_16x16x128_f8f6f4 v[66:69], v[26:33], v[58:65], v[66:69], v216, v216 op_sel_hi:[0,0,0]
	s_setprio 0
	s_barrier
	s_add_i32 s71, s71, 2
	s_add_u32 s36, s36, 0x100
	s_addc_u32 s37, s37, 0
	s_add_u32 s69, s69, 0x100
	s_addc_u32 s70, s70, 0
	s_cmp_gt_u32 s71, 13
	s_cbranch_scc1 .LBB5_1604
.LBB5_1602:
	ds_read_b128 v[18:21], v213
	ds_read_b128 v[26:29], v213 offset:2048
	v_xor_b32_e32 v213, 64, v213
	ds_read_b128 v[22:25], v213
	ds_read_b128 v[30:33], v213 offset:2048
	v_xor_b32_e32 v213, 64, v213
	ds_read_b128 v[2:5], v214
	ds_read_b128 v[10:13], v214 offset:2048
	v_xor_b32_e32 v214, 64, v214
	ds_read_b128 v[6:9], v214
	ds_read_b128 v[14:17], v214 offset:2048
	v_xor_b32_e32 v214, 64, v214
	s_cmp_eq_u32 s71, 12
	s_cselect_b64 s[38:39], -1, 0
	s_add_i32 m0, s44, 0xc000
	s_add_i32 s40, s44, 0xe000
	s_cmp_lg_u32 s71, 12
	v_mov_b32_e32 v194, v204
	ds_read_b128 v[58:61], v215
	ds_read_b128 v[50:53], v215 offset:2048
	ds_read_b128 v[42:45], v215 offset:4096
	ds_read_b128 v[34:37], v215 offset:6144
	v_xor_b32_e32 v215, 64, v215
	ds_read_b128 v[62:65], v215
	ds_read_b128 v[54:57], v215 offset:2048
	ds_read_b128 v[46:49], v215 offset:4096
	ds_read_b128 v[38:41], v215 offset:6144
	s_nop 0
	global_load_lds_dwordx4 v194, s[36:37]
	v_mov_b32_e32 v194, v206
	s_mov_b32 m0, s40
	s_nop 0
	global_load_lds_dwordx4 v194, s[36:37]
	s_cbranch_scc1 .LBB5_1601
	v_mov_b32_e32 v206, v218
	v_mov_b32_e32 v204, v201
	v_mov_b32_e32 v207, v220
	v_mov_b32_e32 v205, v219
	s_branch .LBB5_1601
